# k_agg1: final step gathers exactly the largest remaining neighbour count (1..7 rows) of the wave
# speedup vs baseline: 1.0169x; 1.0041x over previous
.LBB3_4:
	v_sub_u32_e32 v62, v1, v0
	v_cmp_lt_i32_e64 s[18:19], 7, v62
	s_cmp_eq_u64 s[18:19], 0
	s_cbranch_scc0 .Lagg_full
	v_cmp_lt_i32_e64 s[18:19], 6, v62
	s_cmp_eq_u64 s[18:19], 0
	s_cbranch_scc0 .Lagg_n7
	v_cmp_lt_i32_e64 s[18:19], 5, v62
	s_cmp_eq_u64 s[18:19], 0
	s_cbranch_scc0 .Lagg_n6
	v_cmp_lt_i32_e64 s[18:19], 4, v62
	s_cmp_eq_u64 s[18:19], 0
	s_cbranch_scc0 .Lagg_n5
	v_cmp_lt_i32_e64 s[18:19], 3, v62
	s_cmp_eq_u64 s[18:19], 0
	s_cbranch_scc0 .Lagg_n4
	v_cmp_lt_i32_e64 s[18:19], 2, v62
	s_cmp_eq_u64 s[18:19], 0
	s_cbranch_scc0 .Lagg_n3
	v_cmp_lt_i32_e64 s[18:19], 1, v62
	s_cmp_eq_u64 s[18:19], 0
	s_cbranch_scc0 .Lagg_n2
	s_branch .Lagg_n1

.Lagg_n1:
	global_load_dword v30, v[2:3], off
	s_waitcnt vmcnt(0)
	v_lshlrev_b32_sdwa v30, v28, v30 dst_sel:DWORD dst_unused:UNUSED_PAD src0_sel:DWORD src1_sel:WORD_0
	s_nop 0
	v_or_b32_e32 v39, v30, v6
	global_load_dwordx4 v[30:33], v39, s[20:21]
	s_nop 0
	s_waitcnt vmcnt(0)
	v_cvt_f32_f16_e32 v34, v30
	v_cvt_f32_f16_sdwa v35, v30 dst_sel:DWORD dst_unused:UNUSED_PAD src0_sel:WORD_1
	v_cvt_f32_f16_e32 v36, v31
	v_cvt_f32_f16_sdwa v37, v31 dst_sel:DWORD dst_unused:UNUSED_PAD src0_sel:WORD_1
	v_cvt_f32_f16_e32 v38, v32
	v_cvt_f32_f16_sdwa v39, v32 dst_sel:DWORD dst_unused:UNUSED_PAD src0_sel:WORD_1
	v_cvt_f32_f16_e32 v40, v33
	v_cvt_f32_f16_sdwa v41, v33 dst_sel:DWORD dst_unused:UNUSED_PAD src0_sel:WORD_1
	v_pk_add_f32 v[18:19], v[18:19], v[34:35]
	v_pk_add_f32 v[16:17], v[16:17], v[36:37]
	v_pk_add_f32 v[14:15], v[14:15], v[38:39]
	v_pk_add_f32 v[12:13], v[12:13], v[40:41]
	s_branch .Lagg_loop_done
.Lagg_n2:
	global_load_dword v30, v[2:3], off
	s_waitcnt vmcnt(0)
	v_lshlrev_b32_sdwa v34, v28, v30 dst_sel:DWORD dst_unused:UNUSED_PAD src0_sel:DWORD src1_sel:WORD_1
	v_lshlrev_b32_sdwa v30, v28, v30 dst_sel:DWORD dst_unused:UNUSED_PAD src0_sel:DWORD src1_sel:WORD_0
	s_nop 0
	v_or_b32_e32 v39, v30, v6
	v_or_b32_e32 v38, v34, v7
	global_load_dwordx4 v[30:33], v39, s[20:21]
	s_nop 0
	global_load_dwordx4 v[34:37], v38, s[20:21]
	s_nop 0
	s_waitcnt vmcnt(0)
	v_pk_add_f16 v33, v33, v37
	v_pk_add_f16 v32, v32, v36
	v_pk_add_f16 v31, v31, v35
	v_pk_add_f16 v30, v30, v34
	v_cvt_f32_f16_e32 v34, v30
	v_cvt_f32_f16_sdwa v35, v30 dst_sel:DWORD dst_unused:UNUSED_PAD src0_sel:WORD_1
	v_cvt_f32_f16_e32 v36, v31
	v_cvt_f32_f16_sdwa v37, v31 dst_sel:DWORD dst_unused:UNUSED_PAD src0_sel:WORD_1
	v_cvt_f32_f16_e32 v38, v32
	v_cvt_f32_f16_sdwa v39, v32 dst_sel:DWORD dst_unused:UNUSED_PAD src0_sel:WORD_1
	v_cvt_f32_f16_e32 v40, v33
	v_cvt_f32_f16_sdwa v41, v33 dst_sel:DWORD dst_unused:UNUSED_PAD src0_sel:WORD_1
	v_pk_add_f32 v[18:19], v[18:19], v[34:35]
	v_pk_add_f32 v[16:17], v[16:17], v[36:37]
	v_pk_add_f32 v[14:15], v[14:15], v[38:39]
	v_pk_add_f32 v[12:13], v[12:13], v[40:41]
	s_branch .Lagg_loop_done
.Lagg_n3:
	global_load_dwordx2 v[30:31], v[2:3], off
	s_waitcnt vmcnt(0)
	v_lshlrev_b32_sdwa v34, v28, v30 dst_sel:DWORD dst_unused:UNUSED_PAD src0_sel:DWORD src1_sel:WORD_1
	v_lshlrev_b32_sdwa v30, v28, v30 dst_sel:DWORD dst_unused:UNUSED_PAD src0_sel:DWORD src1_sel:WORD_0
	v_lshlrev_b32_sdwa v31, v28, v31 dst_sel:DWORD dst_unused:UNUSED_PAD src0_sel:DWORD src1_sel:WORD_0
	s_nop 0
	v_or_b32_e32 v39, v30, v6
	v_or_b32_e32 v38, v34, v7
	v_or_b32_e32 v40, v31, v6
	global_load_dwordx4 v[30:33], v39, s[20:21]
	s_nop 0
	global_load_dwordx4 v[34:37], v38, s[20:21]
	s_nop 0
	global_load_dwordx4 v[38:41], v40, s[20:21]
	s_nop 0
	s_waitcnt vmcnt(1)
	v_pk_add_f16 v33, v33, v37
	v_pk_add_f16 v32, v32, v36
	v_pk_add_f16 v31, v31, v35
	v_pk_add_f16 v30, v30, v34
	s_waitcnt vmcnt(0)
	v_pk_add_f16 v30, v30, v38
	v_pk_add_f16 v31, v31, v39
	v_pk_add_f16 v32, v32, v40
	v_pk_add_f16 v33, v33, v41
	v_cvt_f32_f16_e32 v34, v30
	v_cvt_f32_f16_sdwa v35, v30 dst_sel:DWORD dst_unused:UNUSED_PAD src0_sel:WORD_1
	v_cvt_f32_f16_e32 v36, v31
	v_cvt_f32_f16_sdwa v37, v31 dst_sel:DWORD dst_unused:UNUSED_PAD src0_sel:WORD_1
	v_cvt_f32_f16_e32 v38, v32
	v_cvt_f32_f16_sdwa v39, v32 dst_sel:DWORD dst_unused:UNUSED_PAD src0_sel:WORD_1
	v_cvt_f32_f16_e32 v40, v33
	v_cvt_f32_f16_sdwa v41, v33 dst_sel:DWORD dst_unused:UNUSED_PAD src0_sel:WORD_1
	v_pk_add_f32 v[18:19], v[18:19], v[34:35]
	v_pk_add_f32 v[16:17], v[16:17], v[36:37]
	v_pk_add_f32 v[14:15], v[14:15], v[38:39]
	v_pk_add_f32 v[12:13], v[12:13], v[40:41]
	s_branch .Lagg_loop_done
.Lagg_n4:
	global_load_dwordx2 v[30:31], v[2:3], off
	s_waitcnt vmcnt(0)
	v_lshlrev_b32_sdwa v34, v28, v30 dst_sel:DWORD dst_unused:UNUSED_PAD src0_sel:DWORD src1_sel:WORD_1
	v_lshlrev_b32_sdwa v30, v28, v30 dst_sel:DWORD dst_unused:UNUSED_PAD src0_sel:DWORD src1_sel:WORD_0
	v_lshlrev_b32_sdwa v35, v28, v31 dst_sel:DWORD dst_unused:UNUSED_PAD src0_sel:DWORD src1_sel:WORD_1
	v_lshlrev_b32_sdwa v31, v28, v31 dst_sel:DWORD dst_unused:UNUSED_PAD src0_sel:DWORD src1_sel:WORD_0
	s_nop 0
	v_or_b32_e32 v39, v30, v6
	v_or_b32_e32 v38, v34, v7
	v_or_b32_e32 v40, v31, v6
	v_or_b32_e32 v42, v35, v7
	global_load_dwordx4 v[30:33], v39, s[20:21]
	s_nop 0
	global_load_dwordx4 v[34:37], v38, s[20:21]
	s_nop 0
	global_load_dwordx4 v[38:41], v40, s[20:21]
	s_nop 0
	global_load_dwordx4 v[42:45], v42, s[20:21]
	s_nop 0
	s_waitcnt vmcnt(2)
	v_pk_add_f16 v33, v33, v37
	v_pk_add_f16 v32, v32, v36
	v_pk_add_f16 v31, v31, v35
	v_pk_add_f16 v30, v30, v34
	s_waitcnt vmcnt(0)
	v_pk_add_f16 v34, v41, v45
	v_pk_add_f16 v35, v40, v44
	v_pk_add_f16 v36, v39, v43
	v_pk_add_f16 v37, v38, v42
	v_pk_add_f16 v30, v30, v37
	v_pk_add_f16 v31, v31, v36
	v_pk_add_f16 v32, v32, v35
	v_pk_add_f16 v33, v33, v34
	v_cvt_f32_f16_e32 v34, v30
	v_cvt_f32_f16_sdwa v35, v30 dst_sel:DWORD dst_unused:UNUSED_PAD src0_sel:WORD_1
	v_cvt_f32_f16_e32 v36, v31
	v_cvt_f32_f16_sdwa v37, v31 dst_sel:DWORD dst_unused:UNUSED_PAD src0_sel:WORD_1
	v_cvt_f32_f16_e32 v38, v32
	v_cvt_f32_f16_sdwa v39, v32 dst_sel:DWORD dst_unused:UNUSED_PAD src0_sel:WORD_1
	v_cvt_f32_f16_e32 v40, v33
	v_cvt_f32_f16_sdwa v41, v33 dst_sel:DWORD dst_unused:UNUSED_PAD src0_sel:WORD_1
	v_pk_add_f32 v[18:19], v[18:19], v[34:35]
	v_pk_add_f32 v[16:17], v[16:17], v[36:37]
	v_pk_add_f32 v[14:15], v[14:15], v[38:39]
	v_pk_add_f32 v[12:13], v[12:13], v[40:41]
	s_branch .Lagg_loop_done
.Lagg_n5:
	global_load_dwordx3 v[30:32], v[2:3], off
	s_waitcnt vmcnt(0)
	v_lshlrev_b32_sdwa v34, v28, v30 dst_sel:DWORD dst_unused:UNUSED_PAD src0_sel:DWORD src1_sel:WORD_1
	v_lshlrev_b32_sdwa v30, v28, v30 dst_sel:DWORD dst_unused:UNUSED_PAD src0_sel:DWORD src1_sel:WORD_0
	v_lshlrev_b32_sdwa v35, v28, v31 dst_sel:DWORD dst_unused:UNUSED_PAD src0_sel:DWORD src1_sel:WORD_1
	v_lshlrev_b32_sdwa v31, v28, v31 dst_sel:DWORD dst_unused:UNUSED_PAD src0_sel:DWORD src1_sel:WORD_0
	v_lshlrev_b32_sdwa v32, v28, v32 dst_sel:DWORD dst_unused:UNUSED_PAD src0_sel:DWORD src1_sel:WORD_0
	s_nop 0
	v_or_b32_e32 v39, v30, v6
	v_or_b32_e32 v38, v34, v7
	v_or_b32_e32 v40, v31, v6
	v_or_b32_e32 v42, v35, v7
	v_or_b32_e32 v46, v32, v6
	global_load_dwordx4 v[30:33], v39, s[20:21]
	s_nop 0
	global_load_dwordx4 v[34:37], v38, s[20:21]
	s_nop 0
	global_load_dwordx4 v[38:41], v40, s[20:21]
	s_nop 0
	global_load_dwordx4 v[42:45], v42, s[20:21]
	s_nop 0
	global_load_dwordx4 v[46:49], v46, s[20:21]
	s_nop 0
	s_waitcnt vmcnt(3)
	v_pk_add_f16 v33, v33, v37
	v_pk_add_f16 v32, v32, v36
	v_pk_add_f16 v31, v31, v35
	v_pk_add_f16 v30, v30, v34
	s_waitcnt vmcnt(1)
	v_pk_add_f16 v34, v41, v45
	v_pk_add_f16 v35, v40, v44
	v_pk_add_f16 v36, v39, v43
	v_pk_add_f16 v37, v38, v42
	v_pk_add_f16 v30, v30, v37
	v_pk_add_f16 v31, v31, v36
	v_pk_add_f16 v32, v32, v35
	v_pk_add_f16 v33, v33, v34
	s_waitcnt vmcnt(0)
	v_pk_add_f16 v30, v30, v46
	v_pk_add_f16 v31, v31, v47
	v_pk_add_f16 v32, v32, v48
	v_pk_add_f16 v33, v33, v49
	v_cvt_f32_f16_e32 v34, v30
	v_cvt_f32_f16_sdwa v35, v30 dst_sel:DWORD dst_unused:UNUSED_PAD src0_sel:WORD_1
	v_cvt_f32_f16_e32 v36, v31
	v_cvt_f32_f16_sdwa v37, v31 dst_sel:DWORD dst_unused:UNUSED_PAD src0_sel:WORD_1
	v_cvt_f32_f16_e32 v38, v32
	v_cvt_f32_f16_sdwa v39, v32 dst_sel:DWORD dst_unused:UNUSED_PAD src0_sel:WORD_1
	v_cvt_f32_f16_e32 v40, v33
	v_cvt_f32_f16_sdwa v41, v33 dst_sel:DWORD dst_unused:UNUSED_PAD src0_sel:WORD_1
	v_pk_add_f32 v[18:19], v[18:19], v[34:35]
	v_pk_add_f32 v[16:17], v[16:17], v[36:37]
	v_pk_add_f32 v[14:15], v[14:15], v[38:39]
	v_pk_add_f32 v[12:13], v[12:13], v[40:41]
	s_branch .Lagg_loop_done
.Lagg_n6:
	global_load_dwordx3 v[30:32], v[2:3], off
	s_waitcnt vmcnt(0)
	v_lshlrev_b32_sdwa v34, v28, v30 dst_sel:DWORD dst_unused:UNUSED_PAD src0_sel:DWORD src1_sel:WORD_1
	v_lshlrev_b32_sdwa v30, v28, v30 dst_sel:DWORD dst_unused:UNUSED_PAD src0_sel:DWORD src1_sel:WORD_0
	v_lshlrev_b32_sdwa v35, v28, v31 dst_sel:DWORD dst_unused:UNUSED_PAD src0_sel:DWORD src1_sel:WORD_1
	v_lshlrev_b32_sdwa v31, v28, v31 dst_sel:DWORD dst_unused:UNUSED_PAD src0_sel:DWORD src1_sel:WORD_0
	v_lshlrev_b32_sdwa v36, v28, v32 dst_sel:DWORD dst_unused:UNUSED_PAD src0_sel:DWORD src1_sel:WORD_1
	v_lshlrev_b32_sdwa v32, v28, v32 dst_sel:DWORD dst_unused:UNUSED_PAD src0_sel:DWORD src1_sel:WORD_0
	s_nop 0
	v_or_b32_e32 v39, v30, v6
	v_or_b32_e32 v38, v34, v7
	v_or_b32_e32 v40, v31, v6
	v_or_b32_e32 v42, v35, v7
	v_or_b32_e32 v46, v32, v6
	v_or_b32_e32 v50, v36, v7
	global_load_dwordx4 v[30:33], v39, s[20:21]
	s_nop 0
	global_load_dwordx4 v[34:37], v38, s[20:21]
	s_nop 0
	global_load_dwordx4 v[38:41], v40, s[20:21]
	s_nop 0
	global_load_dwordx4 v[42:45], v42, s[20:21]
	s_nop 0
	global_load_dwordx4 v[46:49], v46, s[20:21]
	s_nop 0
	global_load_dwordx4 v[50:53], v50, s[20:21]
	s_nop 0
	s_waitcnt vmcnt(4)
	v_pk_add_f16 v33, v33, v37
	v_pk_add_f16 v32, v32, v36
	v_pk_add_f16 v31, v31, v35
	v_pk_add_f16 v30, v30, v34
	s_waitcnt vmcnt(2)
	v_pk_add_f16 v34, v41, v45
	v_pk_add_f16 v35, v40, v44
	v_pk_add_f16 v36, v39, v43
	v_pk_add_f16 v37, v38, v42
	v_pk_add_f16 v30, v30, v37
	v_pk_add_f16 v31, v31, v36
	v_pk_add_f16 v32, v32, v35
	v_pk_add_f16 v33, v33, v34
	s_waitcnt vmcnt(0)
	v_pk_add_f16 v38, v49, v53
	v_pk_add_f16 v39, v48, v52
	v_pk_add_f16 v40, v47, v51
	v_pk_add_f16 v41, v46, v50
	v_pk_add_f16 v30, v30, v41
	v_pk_add_f16 v31, v31, v40
	v_pk_add_f16 v32, v32, v39
	v_pk_add_f16 v33, v33, v38
	v_cvt_f32_f16_e32 v34, v30
	v_cvt_f32_f16_sdwa v35, v30 dst_sel:DWORD dst_unused:UNUSED_PAD src0_sel:WORD_1
	v_cvt_f32_f16_e32 v36, v31
	v_cvt_f32_f16_sdwa v37, v31 dst_sel:DWORD dst_unused:UNUSED_PAD src0_sel:WORD_1
	v_cvt_f32_f16_e32 v38, v32
	v_cvt_f32_f16_sdwa v39, v32 dst_sel:DWORD dst_unused:UNUSED_PAD src0_sel:WORD_1
	v_cvt_f32_f16_e32 v40, v33
	v_cvt_f32_f16_sdwa v41, v33 dst_sel:DWORD dst_unused:UNUSED_PAD src0_sel:WORD_1
	v_pk_add_f32 v[18:19], v[18:19], v[34:35]
	v_pk_add_f32 v[16:17], v[16:17], v[36:37]
	v_pk_add_f32 v[14:15], v[14:15], v[38:39]
	v_pk_add_f32 v[12:13], v[12:13], v[40:41]
	s_branch .Lagg_loop_done
.Lagg_n7:
	global_load_dwordx4 v[30:33], v[2:3], off
	s_waitcnt vmcnt(0)
	v_lshlrev_b32_sdwa v34, v28, v30 dst_sel:DWORD dst_unused:UNUSED_PAD src0_sel:DWORD src1_sel:WORD_1
	v_lshlrev_b32_sdwa v30, v28, v30 dst_sel:DWORD dst_unused:UNUSED_PAD src0_sel:DWORD src1_sel:WORD_0
	v_lshlrev_b32_sdwa v35, v28, v31 dst_sel:DWORD dst_unused:UNUSED_PAD src0_sel:DWORD src1_sel:WORD_1
	v_lshlrev_b32_sdwa v31, v28, v31 dst_sel:DWORD dst_unused:UNUSED_PAD src0_sel:DWORD src1_sel:WORD_0
	v_lshlrev_b32_sdwa v36, v28, v32 dst_sel:DWORD dst_unused:UNUSED_PAD src0_sel:DWORD src1_sel:WORD_1
	v_lshlrev_b32_sdwa v32, v28, v32 dst_sel:DWORD dst_unused:UNUSED_PAD src0_sel:DWORD src1_sel:WORD_0
	v_lshlrev_b32_sdwa v33, v28, v33 dst_sel:DWORD dst_unused:UNUSED_PAD src0_sel:DWORD src1_sel:WORD_0
	s_nop 0
	v_or_b32_e32 v39, v30, v6
	v_or_b32_e32 v38, v34, v7
	v_or_b32_e32 v40, v31, v6
	v_or_b32_e32 v42, v35, v7
	v_or_b32_e32 v46, v32, v6
	v_or_b32_e32 v50, v36, v7
	v_or_b32_e32 v54, v33, v6
	global_load_dwordx4 v[30:33], v39, s[20:21]
	s_nop 0
	global_load_dwordx4 v[34:37], v38, s[20:21]
	s_nop 0
	global_load_dwordx4 v[38:41], v40, s[20:21]
	s_nop 0
	global_load_dwordx4 v[42:45], v42, s[20:21]
	s_nop 0
	global_load_dwordx4 v[46:49], v46, s[20:21]
	s_nop 0
	global_load_dwordx4 v[50:53], v50, s[20:21]
	s_nop 0
	global_load_dwordx4 v[54:57], v54, s[20:21]
	s_nop 0
	s_waitcnt vmcnt(5)
	v_pk_add_f16 v33, v33, v37
	v_pk_add_f16 v32, v32, v36
	v_pk_add_f16 v31, v31, v35
	v_pk_add_f16 v30, v30, v34
	s_waitcnt vmcnt(3)
	v_pk_add_f16 v34, v41, v45
	v_pk_add_f16 v35, v40, v44
	v_pk_add_f16 v36, v39, v43
	v_pk_add_f16 v37, v38, v42
	v_pk_add_f16 v30, v30, v37
	v_pk_add_f16 v31, v31, v36
	v_pk_add_f16 v32, v32, v35
	v_pk_add_f16 v33, v33, v34
	s_waitcnt vmcnt(1)
	v_pk_add_f16 v38, v49, v53
	v_pk_add_f16 v39, v48, v52
	v_pk_add_f16 v40, v47, v51
	v_pk_add_f16 v41, v46, v50
	s_waitcnt vmcnt(0)
	v_pk_add_f16 v41, v41, v54
	v_pk_add_f16 v40, v40, v55
	v_pk_add_f16 v39, v39, v56
	v_pk_add_f16 v38, v38, v57
	v_pk_add_f16 v30, v30, v41
	v_pk_add_f16 v31, v31, v40
	v_pk_add_f16 v32, v32, v39
	v_pk_add_f16 v33, v33, v38
	v_cvt_f32_f16_e32 v34, v30
	v_cvt_f32_f16_sdwa v35, v30 dst_sel:DWORD dst_unused:UNUSED_PAD src0_sel:WORD_1
	v_cvt_f32_f16_e32 v36, v31
	v_cvt_f32_f16_sdwa v37, v31 dst_sel:DWORD dst_unused:UNUSED_PAD src0_sel:WORD_1
	v_cvt_f32_f16_e32 v38, v32
	v_cvt_f32_f16_sdwa v39, v32 dst_sel:DWORD dst_unused:UNUSED_PAD src0_sel:WORD_1
	v_cvt_f32_f16_e32 v40, v33
	v_cvt_f32_f16_sdwa v41, v33 dst_sel:DWORD dst_unused:UNUSED_PAD src0_sel:WORD_1
	v_pk_add_f32 v[18:19], v[18:19], v[34:35]
	v_pk_add_f32 v[16:17], v[16:17], v[36:37]
	v_pk_add_f32 v[14:15], v[14:15], v[38:39]
	v_pk_add_f32 v[12:13], v[12:13], v[40:41]
	s_branch .Lagg_loop_done
